# v070
# baseline (speedup 1.0000x reference)
.LBB1_2:
	s_waitcnt lgkmcnt(0)
	v_lshl_add_u64 v[6:7], s[6:7], 0, v[2:3]
	global_load_dwordx4 v[6:9], v[6:7], off
	v_add_u32_e32 v4, s2, v4
	v_cmp_lt_i32_e32 vcc, s3, v4
	v_lshl_add_u64 v[10:11], s[10:11], 0, v[2:3]
	v_lshl_add_u64 v[2:3], v[2:3], 0, s[12:13]
	s_or_b64 s[14:15], vcc, s[14:15]
	s_waitcnt vmcnt(0)
	global_store_dwordx4 v[10:11], v[6:9], off sc1
	s_andn2_b64 exec, exec, s[14:15]
	s_cbranch_execnz .LBB1_2

.LBB1_5:
	s_waitcnt lgkmcnt(0)
	v_lshl_add_u64 v[8:9], s[4:5], 0, v[2:3]
	global_load_dwordx4 v[8:11], v[8:9], off
	v_and_b32_e32 v7, 0xfffffc00, v6
	v_add_u32_e32 v6, s2, v6
	v_cmp_eq_u32_e32 vcc, s3, v7
	v_lshl_add_u64 v[12:13], s[12:13], 0, v[2:3]
	v_lshl_add_u64 v[2:3], v[2:3], 0, s[14:15]
	v_cndmask_b32_e32 v14, v4, v5, vcc
	v_cmp_lt_i32_e32 vcc, s18, v6
	s_or_b64 s[16:17], vcc, s[16:17]
	s_waitcnt vmcnt(0)
	v_pk_mul_f32 v[10:11], v[14:15], v[10:11] op_sel_hi:[0,1]
	v_pk_mul_f32 v[8:9], v[14:15], v[8:9] op_sel_hi:[0,1]
	global_store_dwordx4 v[12:13], v[8:11], off sc1
	s_andn2_b64 exec, exec, s[16:17]
	s_cbranch_execnz .LBB1_5

.LBB1_8:
	v_lshl_add_u64 v[8:9], s[6:7], 0, v[2:3]
	global_load_dwordx4 v[8:11], v[8:9], off
	v_and_b32_e32 v7, 0xffffff00, v6
	v_add_u32_e32 v6, s2, v6
	v_cmp_eq_u32_e32 vcc, s3, v7
	v_lshl_add_u64 v[12:13], s[4:5], 0, v[2:3]
	v_lshl_add_u64 v[2:3], v[2:3], 0, s[12:13]
	v_cndmask_b32_e32 v14, v4, v5, vcc
	v_cmp_lt_i32_e32 vcc, s16, v6
	s_or_b64 s[14:15], vcc, s[14:15]
	s_waitcnt vmcnt(0)
	v_pk_mul_f32 v[10:11], v[14:15], v[10:11] op_sel_hi:[0,1]
	v_pk_mul_f32 v[8:9], v[14:15], v[8:9] op_sel_hi:[0,1]
	global_store_dwordx4 v[12:13], v[8:11], off sc1
	s_andn2_b64 exec, exec, s[14:15]
	s_cbranch_execnz .LBB1_8

.LBB1_11:
	v_lshl_add_u64 v[6:7], s[10:11], 0, v[2:3]
	global_load_dwordx4 v[6:9], v[6:7], off
	v_and_b32_e32 v5, 0x300, v0
	v_add_u32_e32 v0, s2, v0
	v_cmp_eq_u32_e32 vcc, s3, v5
	v_lshl_add_u64 v[10:11], s[0:1], 0, v[2:3]
	v_lshl_add_u64 v[2:3], v[2:3], 0, s[4:5]
	v_cndmask_b32_e32 v12, v1, v4, vcc
	v_cmp_lt_i32_e32 vcc, s8, v0
	s_or_b64 s[6:7], vcc, s[6:7]
	s_waitcnt vmcnt(0)
	v_pk_mul_f32 v[8:9], v[12:13], v[8:9] op_sel_hi:[0,1]
	v_pk_mul_f32 v[6:7], v[12:13], v[6:7] op_sel_hi:[0,1]
	global_store_dwordx4 v[10:11], v[6:9], off sc1
	s_andn2_b64 exec, exec, s[6:7]
	s_cbranch_execnz .LBB1_11

.LBB4_29:
	s_or_b64 exec, exec, s[10:11]
	v_pk_mul_f32 v[18:19], v[60:61], v[34:35] op_sel:[1,0] op_sel_hi:[0,1]
	v_pk_mul_f32 v[20:21], v[58:59], v[32:33]
	v_add_f32_e32 v18, v18, v19
	v_add_f32_e32 v18, v21, v18
	v_add_f32_e32 v18, v20, v18
	v_add_f32_e32 v22, v22, v18
	v_pk_mul_f32 v[18:19], v[60:61], v[38:39] op_sel:[1,0] op_sel_hi:[0,1]
	v_pk_mul_f32 v[20:21], v[58:59], v[30:31]
	v_add_f32_e32 v18, v18, v19
	v_add_f32_e32 v18, v21, v18
	v_add_f32_e32 v18, v20, v18
	v_add_f32_e32 v23, v23, v18
	v_pk_mul_f32 v[18:19], v[60:61], v[46:47] op_sel:[1,0] op_sel_hi:[0,1]
	v_pk_mul_f32 v[20:21], v[58:59], v[28:29]
	v_add_f32_e32 v18, v18, v19
	v_add_f32_e32 v18, v21, v18
	v_add_f32_e32 v18, v20, v18
	v_add_f32_e32 v24, v24, v18
	v_pk_mul_f32 v[18:19], v[60:61], v[50:51] op_sel:[1,0] op_sel_hi:[0,1]
	v_pk_mul_f32 v[20:21], v[58:59], v[26:27]
	v_add_f32_e32 v18, v18, v19
	v_add_f32_e32 v19, v21, v18
	v_mul_f32_e32 v21, 0xbfb8aa3b, v22
	v_mul_f32_e32 v22, -2.0, v24
	v_mul_f32_e32 v22, 0x3fb8aa3b, v22
	v_mul_f32_e32 v18, 0xbfb8aa3b, v23
	v_exp_f32_e32 v22, v22
	v_exp_f32_e32 v18, v18
	v_exp_f32_e32 v21, v21
	v_add_f32_e32 v19, v20, v19
	v_add_f32_e32 v22, 1.0, v22
	v_add_f32_e32 v18, 1.0, v18
	v_add_f32_e32 v21, 1.0, v21
	v_rcp_f32_e32 v22, v22
	v_rcp_f32_e32 v18, v18
	v_rcp_f32_e32 v53, v21
	v_add_f32_e32 v20, v25, v19
	v_fma_f32 v19, v22, 2.0, -1.0
	v_pk_mul_f32 v[18:19], v[52:53], v[18:19]
	s_nop 0
	v_add_f32_e32 v52, v18, v19
	v_mul_f32_e32 v19, -2.0, v52
	v_mul_f32_e32 v19, 0x3fb8aa3b, v19
	v_mul_f32_e32 v18, 0xbfb8aa3b, v20
	v_exp_f32_e32 v19, v19
	v_exp_f32_e32 v18, v18
	v_add_f32_e32 v19, 1.0, v19
	v_add_f32_e32 v18, 1.0, v18
	v_rcp_f32_e32 v19, v19
	v_rcp_f32_e32 v18, v18
	v_fma_f32 v19, v19, 2.0, -1.0
	v_mul_f32_e32 v18, v18, v19
	s_nop 1
	v_mov_b32_dpp v61, v18 quad_perm:[0,0,0,0] row_mask:0xf bank_mask:0xf bound_ctrl:1
	v_mov_b32_dpp v60, v18 quad_perm:[1,1,1,1] row_mask:0xf bank_mask:0xf bound_ctrl:1
	v_mov_b32_dpp v59, v18 quad_perm:[2,2,2,2] row_mask:0xf bank_mask:0xf bound_ctrl:1
	v_mov_b32_dpp v58, v18 quad_perm:[3,3,3,3] row_mask:0xf bank_mask:0xf bound_ctrl:1
	s_and_saveexec_b64 s[10:11], s[0:1]
	s_xor_b64 s[10:11], exec, s[10:11]
	s_cbranch_execz .LBB4_31
	v_lshl_add_u64 v[20:21], v[10:11], 2, v[12:13]
	global_store_dword v[20:21], v18, off sc1

.LBB5_11:
	v_add_u32_e32 v7, s0, v10
	ds_read2st64_b32 v[22:23], v5 offset1:1
	ds_read2st64_b32 v[24:25], v5 offset0:2 offset1:3
	ds_read2st64_b32 v[26:27], v5 offset0:4 offset1:5
	ds_read2st64_b32 v[28:29], v5 offset0:6 offset1:7
	ds_read_b128 v[14:17], v7
	ds_read_b128 v[18:21], v7 offset:16
	s_add_i32 s0, s0, 32
	v_add_u32_e32 v5, 0x800, v5
	s_cmpk_eq_i32 s0, 0x1c0
	s_waitcnt lgkmcnt(1)
	v_fmac_f32_e32 v4, v22, v14
	v_fmac_f32_e32 v4, v23, v15
	v_fmac_f32_e32 v4, v24, v16
	v_fmac_f32_e32 v4, v25, v17
	s_waitcnt lgkmcnt(0)
	v_fmac_f32_e32 v4, v26, v18
	v_fmac_f32_e32 v4, v27, v19
	v_fmac_f32_e32 v4, v28, v20
	v_fmac_f32_e32 v4, v29, v21
	s_cbranch_scc0 .LBB5_11
	v_mbcnt_lo_u32_b32 v5, -1, 0
	v_mbcnt_hi_u32_b32 v5, -1, v5
	v_mov_b32_e32 v13, 0x80
	v_mul_f32_e32 v7, v9, v4
	v_lshl_or_b32 v13, v5, 2, v13
	ds_bpermute_b32 v7, v13, v7
	v_and_b32_e32 v18, 63, v5
	v_cmp_gt_u32_e32 vcc, 48, v18
	s_waitcnt lgkmcnt(0)
	v_fmac_f32_e32 v7, v9, v4
	v_cndmask_b32_e64 v4, 0, 16, vcc
	v_add_lshl_u32 v14, v4, v5, 2
	ds_bpermute_b32 v4, v14, v7
	v_cmp_gt_u32_e32 vcc, 56, v18
	s_waitcnt lgkmcnt(0)
	v_add_f32_e32 v4, v7, v4
	v_cndmask_b32_e64 v15, 0, 8, vcc
	v_add_lshl_u32 v15, v15, v5, 2
	ds_bpermute_b32 v7, v15, v4
	v_cmp_gt_u32_e32 vcc, 60, v18
	s_waitcnt lgkmcnt(0)
	v_add_f32_e32 v4, v4, v7
	v_cndmask_b32_e64 v16, 0, 4, vcc
	v_add_lshl_u32 v16, v16, v5, 2
	ds_bpermute_b32 v7, v16, v4
	v_cmp_gt_u32_e32 vcc, 62, v18
	s_waitcnt lgkmcnt(0)
	v_add_f32_e32 v4, v4, v7
	v_cndmask_b32_e64 v17, 0, 2, vcc
	v_add_lshl_u32 v17, v17, v5, 2
	ds_bpermute_b32 v7, v17, v4
	v_cmp_ne_u32_e32 vcc, 63, v18
	s_waitcnt lgkmcnt(0)
	v_add_f32_e32 v7, v4, v7
	v_addc_co_u32_e32 v5, vcc, 0, v5, vcc
	v_lshlrev_b32_e32 v18, 2, v5
	ds_bpermute_b32 v19, v18, v7
	v_cmp_eq_u32_e32 vcc, 0, v6
	v_lshl_add_u64 v[4:5], v[0:1], 2, s[14:15]
	s_and_saveexec_b64 s[0:1], vcc
	s_cbranch_execz .LBB5_14
	s_waitcnt lgkmcnt(0)
	v_add_f32_e32 v1, v7, v19
	v_add_f32_e32 v1, s8, v1
	global_store_dword v[4:5], v1, off sc1

.LBB5_17:
	v_add_u32_e32 v7, s0, v10
	ds_read2st64_b32 v[28:29], v6 offset1:1
	ds_read2st64_b32 v[30:31], v6 offset0:2 offset1:3
	ds_read2st64_b32 v[32:33], v6 offset0:4 offset1:5
	ds_read2st64_b32 v[34:35], v6 offset0:6 offset1:7
	ds_read_b128 v[20:23], v7
	ds_read_b128 v[24:27], v7 offset:16
	s_add_i32 s0, s0, 32
	v_add_u32_e32 v6, 0x800, v6
	s_cmpk_lg_i32 s0, 0x1c0
	s_waitcnt lgkmcnt(1)
	v_fmac_f32_e32 v1, v28, v20
	v_fmac_f32_e32 v1, v29, v21
	v_fmac_f32_e32 v1, v30, v22
	v_fmac_f32_e32 v1, v31, v23
	s_waitcnt lgkmcnt(0)
	v_fmac_f32_e32 v1, v32, v24
	v_fmac_f32_e32 v1, v33, v25
	v_fmac_f32_e32 v1, v34, v26
	v_fmac_f32_e32 v1, v35, v27
	s_cbranch_scc1 .LBB5_17
	v_mul_f32_e32 v6, v9, v1
	ds_bpermute_b32 v6, v13, v6
	s_waitcnt lgkmcnt(0)
	v_fmac_f32_e32 v6, v9, v1
	ds_bpermute_b32 v1, v14, v6
	s_waitcnt lgkmcnt(0)
	v_add_f32_e32 v1, v6, v1
	ds_bpermute_b32 v6, v15, v1
	s_waitcnt lgkmcnt(0)
	v_add_f32_e32 v1, v1, v6
	ds_bpermute_b32 v6, v16, v1
	s_waitcnt lgkmcnt(0)
	v_add_f32_e32 v1, v1, v6
	ds_bpermute_b32 v6, v17, v1
	s_waitcnt lgkmcnt(0)
	v_add_f32_e32 v1, v1, v6
	ds_bpermute_b32 v6, v18, v1
	s_and_saveexec_b64 s[0:1], vcc
	s_cbranch_execz .LBB5_20
	s_waitcnt lgkmcnt(0)
	v_add_f32_e32 v1, v1, v6
	v_add_f32_e32 v1, s8, v1
	global_store_dword v[4:5], v1, off offset:16 sc1

.LBB5_23:
	v_add_u32_e32 v7, s0, v10
	ds_read2st64_b32 v[28:29], v6 offset1:1
	ds_read2st64_b32 v[30:31], v6 offset0:2 offset1:3
	ds_read2st64_b32 v[32:33], v6 offset0:4 offset1:5
	ds_read2st64_b32 v[34:35], v6 offset0:6 offset1:7
	ds_read_b128 v[20:23], v7
	ds_read_b128 v[24:27], v7 offset:16
	s_add_i32 s0, s0, 32
	v_add_u32_e32 v6, 0x800, v6
	s_cmpk_lg_i32 s0, 0x1c0
	s_waitcnt lgkmcnt(1)
	v_fmac_f32_e32 v1, v28, v20
	v_fmac_f32_e32 v1, v29, v21
	v_fmac_f32_e32 v1, v30, v22
	v_fmac_f32_e32 v1, v31, v23
	s_waitcnt lgkmcnt(0)
	v_fmac_f32_e32 v1, v32, v24
	v_fmac_f32_e32 v1, v33, v25
	v_fmac_f32_e32 v1, v34, v26
	v_fmac_f32_e32 v1, v35, v27
	s_cbranch_scc1 .LBB5_23
	v_mul_f32_e32 v6, v9, v1
	ds_bpermute_b32 v6, v13, v6
	s_waitcnt lgkmcnt(0)
	v_fmac_f32_e32 v6, v9, v1
	ds_bpermute_b32 v1, v14, v6
	s_waitcnt lgkmcnt(0)
	v_add_f32_e32 v1, v6, v1
	ds_bpermute_b32 v6, v15, v1
	s_waitcnt lgkmcnt(0)
	v_add_f32_e32 v1, v1, v6
	ds_bpermute_b32 v6, v16, v1
	s_waitcnt lgkmcnt(0)
	v_add_f32_e32 v1, v1, v6
	ds_bpermute_b32 v6, v17, v1
	s_waitcnt lgkmcnt(0)
	v_add_f32_e32 v1, v1, v6
	ds_bpermute_b32 v6, v18, v1
	s_and_saveexec_b64 s[0:1], vcc
	s_cbranch_execz .LBB5_26
	s_waitcnt lgkmcnt(0)
	v_add_f32_e32 v1, v1, v6
	v_add_f32_e32 v1, s8, v1
	global_store_dword v[4:5], v1, off offset:32 sc1

.LBB5_29:
	v_add_u32_e32 v3, s0, v10
	ds_read2st64_b32 v[0:1], v2 offset1:1
	ds_read2st64_b32 v[6:7], v2 offset0:2 offset1:3
	ds_read2st64_b32 v[28:29], v2 offset0:4 offset1:5
	ds_read2st64_b32 v[30:31], v2 offset0:6 offset1:7
	ds_read_b128 v[20:23], v3
	ds_read_b128 v[24:27], v3 offset:16
	s_add_i32 s0, s0, 32
	v_add_u32_e32 v2, 0x800, v2
	s_cmpk_lg_i32 s0, 0x1c0
	s_waitcnt lgkmcnt(1)
	v_fmac_f32_e32 v8, v0, v20
	v_fmac_f32_e32 v8, v1, v21
	v_fmac_f32_e32 v8, v6, v22
	v_fmac_f32_e32 v8, v7, v23
	s_waitcnt lgkmcnt(0)
	v_fmac_f32_e32 v8, v28, v24
	v_fmac_f32_e32 v8, v29, v25
	v_fmac_f32_e32 v8, v30, v26
	v_fmac_f32_e32 v8, v31, v27
	s_cbranch_scc1 .LBB5_29
	v_mul_f32_e32 v0, v9, v8
	ds_bpermute_b32 v0, v13, v0
	s_waitcnt lgkmcnt(0)
	v_fmac_f32_e32 v0, v9, v8
	ds_bpermute_b32 v1, v14, v0
	s_waitcnt lgkmcnt(0)
	v_add_f32_e32 v0, v0, v1
	ds_bpermute_b32 v1, v15, v0
	s_waitcnt lgkmcnt(0)
	v_add_f32_e32 v0, v0, v1
	ds_bpermute_b32 v1, v16, v0
	s_waitcnt lgkmcnt(0)
	v_add_f32_e32 v0, v0, v1
	ds_bpermute_b32 v1, v17, v0
	s_waitcnt lgkmcnt(0)
	v_add_f32_e32 v0, v0, v1
	ds_bpermute_b32 v1, v18, v0
	s_and_saveexec_b64 s[0:1], vcc
	s_cbranch_execz .LBB5_32
	s_waitcnt lgkmcnt(0)
	v_add_f32_e32 v0, v0, v1
	v_add_f32_e32 v0, s8, v0
	global_store_dword v[4:5], v0, off offset:48 sc1
